# speedup vs baseline: 1.0426x; 1.0090x over previous
.LBB1_27:
	s_or_b64 exec, exec, s[0:1]
	v_mul_lo_u16_e32 v2, 0x56, v66
	v_mov_b32_e32 v3, 3
	v_mul_lo_u16_sdwa v2, v2, v3 dst_sel:DWORD dst_unused:UNUSED_PAD src0_sel:BYTE_1 src1_sel:DWORD
	v_sub_u16_e32 v2, v66, v2
	v_mov_b32_e32 v4, 0
	v_cmp_eq_u16_sdwa s[0:1], v2, v4 src0_sel:BYTE_0 src1_sel:DWORD
	v_and_b32_e32 v168, 31, v0
	v_lshrrev_b32_e32 v174, 5, v67
	v_cndmask_b32_e64 v19, 32, 0, s[0:1]
	v_or_b32_e32 v4, v19, v168
	v_cndmask_b32_e64 v5, v165, v166, s[4:5]
	v_mul_u32_u24_e32 v4, 0x190, v4
	v_lshlrev_b32_e32 v169, 4, v174
	v_add3_u32 v32, v5, v4, v169
	v_mov_b32_e32 v3, 2
	ds_read_b128 v[20:23], v32
	v_cmp_eq_u16_sdwa s[0:1], v2, v3 src0_sel:BYTE_0 src1_sel:DWORD
	v_lshlrev_b32_e32 v171, 2, v174
	v_or_b32_e32 v19, v19, v171
	v_cndmask_b32_e64 v2, 0, 32, s[0:1]
	v_or_b32_e32 v18, v2, v168
	v_mul_u32_u24_e32 v2, 0x190, v18
	v_add3_u32 v33, v166, v2, v169
	ds_read_b128 v[24:27], v33
	v_add_u32_e32 v170, 0x1bc00, v173
	v_add_u32_e32 v175, 0x20000, v173
	s_movk_i32 s3, 0x110
	v_lshlrev_b32_e32 v226, 2, v19
	v_lshlrev_b32_e32 v227, 2, v18
	v_add_u32_e32 v228, v164, v226
	v_add_u32_e32 v229, v164, v227
	v_mov_b32_e32 v230, 0x100
	v_cndmask_b32_e64 v230, 0, v230, s[4:5]
	v_add3_u32 v230, v167, v230, v226
	v_add_u32_e32 v231, v167, v227
	ds_read_b32 v224, v229
	ds_read_b32 v225, v231 offset:256
	ds_read_b128 v[176:179], v228 offset:0
	ds_read_b128 v[180:183], v228 offset:32
	ds_read_b128 v[184:187], v228 offset:64
	ds_read_b128 v[188:191], v228 offset:96
	ds_read_b128 v[192:195], v230 offset:0
	ds_read_b128 v[196:199], v230 offset:32
	ds_read_b128 v[200:203], v230 offset:64
	ds_read_b128 v[204:207], v230 offset:96
	ds_read_b128 v[28:31], v32 offset:32
	ds_read_b128 v[120:123], v33 offset:32
	s_waitcnt lgkmcnt(12)
	v_mfma_f32_32x32x2_f32 v[2:17], v20, v24, 0
	v_mfma_f32_32x32x2_f32 v[2:17], v21, v25, v[2:17]
	v_mfma_f32_32x32x2_f32 v[2:17], v22, v26, v[2:17]
	v_mfma_f32_32x32x2_f32 v[2:17], v23, v27, v[2:17]
	ds_read_b128 v[20:23], v32 offset:64
	ds_read_b128 v[24:27], v33 offset:64
	s_waitcnt lgkmcnt(2)
	v_mfma_f32_32x32x2_f32 v[2:17], v28, v120, v[2:17]
	v_sub_f32_e32 v176, v176, v224
	v_min_f32_e32 v176, 0, v176
	v_mul_f32_e32 v176, 0x3fb8aa3b, v176
	v_exp_f32_e32 v176, v176
	v_mfma_f32_32x32x2_f32 v[2:17], v29, v121, v[2:17]
	v_mov_b32_e32 v226, v19
	v_mul_f32_e32 v176, v192, v176
	v_cmp_le_u32_e32 vcc, v18, v226
	v_mul_f32_e32 v176, v225, v176
	v_mfma_f32_32x32x2_f32 v[2:17], v30, v122, v[2:17]
	s_nop 0
	v_cndmask_b32_e32 v176, 0, v176, vcc
	v_sub_f32_e32 v177, v177, v224
	v_min_f32_e32 v177, 0, v177
	v_mfma_f32_32x32x2_f32 v[2:17], v31, v123, v[2:17]
	v_mul_f32_e32 v177, 0x3fb8aa3b, v177
	v_exp_f32_e32 v177, v177
	v_or_b32_e32 v226, 1, v19
	v_mul_f32_e32 v177, v193, v177
	ds_read_b128 v[28:31], v32 offset:96
	ds_read_b128 v[120:123], v33 offset:96
	s_waitcnt lgkmcnt(2)
	v_mfma_f32_32x32x2_f32 v[2:17], v20, v24, v[2:17]
	v_cmp_le_u32_e32 vcc, v18, v226
	v_mul_f32_e32 v177, v225, v177
	s_nop 0
	v_cndmask_b32_e32 v177, 0, v177, vcc
	v_mfma_f32_32x32x2_f32 v[2:17], v21, v25, v[2:17]
	v_sub_f32_e32 v178, v178, v224
	v_min_f32_e32 v178, 0, v178
	v_mul_f32_e32 v178, 0x3fb8aa3b, v178
	v_exp_f32_e32 v178, v178
	v_mfma_f32_32x32x2_f32 v[2:17], v22, v26, v[2:17]
	v_or_b32_e32 v226, 2, v19
	v_mul_f32_e32 v178, v194, v178
	v_cmp_le_u32_e32 vcc, v18, v226
	v_mul_f32_e32 v178, v225, v178
	v_mfma_f32_32x32x2_f32 v[2:17], v23, v27, v[2:17]
	s_nop 0
	v_cndmask_b32_e32 v178, 0, v178, vcc
	v_sub_f32_e32 v179, v179, v224
	v_min_f32_e32 v179, 0, v179
	ds_read_b128 v[20:23], v32 offset:128
	ds_read_b128 v[24:27], v33 offset:128
	s_waitcnt lgkmcnt(2)
	v_mfma_f32_32x32x2_f32 v[2:17], v28, v120, v[2:17]
	v_mul_f32_e32 v179, 0x3fb8aa3b, v179
	v_exp_f32_e32 v179, v179
	v_or_b32_e32 v226, 3, v19
	v_mul_f32_e32 v179, v195, v179
	v_mfma_f32_32x32x2_f32 v[2:17], v29, v121, v[2:17]
	v_cmp_le_u32_e32 vcc, v18, v226
	v_mul_f32_e32 v179, v225, v179
	s_nop 0
	v_cndmask_b32_e32 v179, 0, v179, vcc
	v_mfma_f32_32x32x2_f32 v[2:17], v30, v122, v[2:17]
	v_sub_f32_e32 v180, v180, v224
	v_min_f32_e32 v180, 0, v180
	v_mul_f32_e32 v180, 0x3fb8aa3b, v180
	v_exp_f32_e32 v180, v180
	v_mfma_f32_32x32x2_f32 v[2:17], v31, v123, v[2:17]
	v_or_b32_e32 v226, 8, v19
	v_mul_f32_e32 v180, v196, v180
	v_cmp_le_u32_e32 vcc, v18, v226
	v_mul_f32_e32 v180, v225, v180
	ds_read_b128 v[28:31], v32 offset:160
	ds_read_b128 v[120:123], v33 offset:160
	s_waitcnt lgkmcnt(2)
	v_mfma_f32_32x32x2_f32 v[2:17], v20, v24, v[2:17]
	s_nop 0
	v_cndmask_b32_e32 v180, 0, v180, vcc
	v_sub_f32_e32 v181, v181, v224
	v_min_f32_e32 v181, 0, v181
	v_mfma_f32_32x32x2_f32 v[2:17], v21, v25, v[2:17]
	v_mul_f32_e32 v181, 0x3fb8aa3b, v181
	v_exp_f32_e32 v181, v181
	v_or_b32_e32 v226, 9, v19
	v_mul_f32_e32 v181, v197, v181
	v_mfma_f32_32x32x2_f32 v[2:17], v22, v26, v[2:17]
	v_cmp_le_u32_e32 vcc, v18, v226
	v_mul_f32_e32 v181, v225, v181
	s_nop 0
	v_cndmask_b32_e32 v181, 0, v181, vcc
	v_mfma_f32_32x32x2_f32 v[2:17], v23, v27, v[2:17]
	v_sub_f32_e32 v182, v182, v224
	v_min_f32_e32 v182, 0, v182
	v_mul_f32_e32 v182, 0x3fb8aa3b, v182
	v_exp_f32_e32 v182, v182
	ds_read_b128 v[20:23], v32 offset:192
	ds_read_b128 v[24:27], v33 offset:192
	s_waitcnt lgkmcnt(2)
	v_mfma_f32_32x32x2_f32 v[2:17], v28, v120, v[2:17]
	v_or_b32_e32 v226, 10, v19
	v_mul_f32_e32 v182, v198, v182
	v_cmp_le_u32_e32 vcc, v18, v226
	v_mul_f32_e32 v182, v225, v182
	v_mfma_f32_32x32x2_f32 v[2:17], v29, v121, v[2:17]
	s_nop 0
	v_cndmask_b32_e32 v182, 0, v182, vcc
	v_sub_f32_e32 v183, v183, v224
	v_min_f32_e32 v183, 0, v183
	v_mfma_f32_32x32x2_f32 v[2:17], v30, v122, v[2:17]
	v_mul_f32_e32 v183, 0x3fb8aa3b, v183
	v_exp_f32_e32 v183, v183
	v_or_b32_e32 v226, 11, v19
	v_mul_f32_e32 v183, v199, v183
	v_mfma_f32_32x32x2_f32 v[2:17], v31, v123, v[2:17]
	v_cmp_le_u32_e32 vcc, v18, v226
	v_mul_f32_e32 v183, v225, v183
	s_nop 0
	v_cndmask_b32_e32 v183, 0, v183, vcc
	ds_read_b128 v[28:31], v32 offset:224
	ds_read_b128 v[120:123], v33 offset:224
	s_waitcnt lgkmcnt(2)
	v_mfma_f32_32x32x2_f32 v[2:17], v20, v24, v[2:17]
	v_sub_f32_e32 v184, v184, v224
	v_min_f32_e32 v184, 0, v184
	v_mul_f32_e32 v184, 0x3fb8aa3b, v184
	v_exp_f32_e32 v184, v184
	v_mfma_f32_32x32x2_f32 v[2:17], v21, v25, v[2:17]
	v_or_b32_e32 v226, 16, v19
	v_mul_f32_e32 v184, v200, v184
	v_cmp_le_u32_e32 vcc, v18, v226
	v_mul_f32_e32 v184, v225, v184
	v_mfma_f32_32x32x2_f32 v[2:17], v22, v26, v[2:17]
	s_nop 0
	v_cndmask_b32_e32 v184, 0, v184, vcc
	v_sub_f32_e32 v185, v185, v224
	v_min_f32_e32 v185, 0, v185
	v_mfma_f32_32x32x2_f32 v[2:17], v23, v27, v[2:17]
	v_mul_f32_e32 v185, 0x3fb8aa3b, v185
	v_exp_f32_e32 v185, v185
	v_or_b32_e32 v226, 17, v19
	v_mul_f32_e32 v185, v201, v185
	ds_read_b128 v[20:23], v32 offset:256
	ds_read_b128 v[24:27], v33 offset:256
	s_waitcnt lgkmcnt(2)
	v_mfma_f32_32x32x2_f32 v[2:17], v28, v120, v[2:17]
	v_cmp_le_u32_e32 vcc, v18, v226
	v_mul_f32_e32 v185, v225, v185
	s_nop 0
	v_cndmask_b32_e32 v185, 0, v185, vcc
	v_mfma_f32_32x32x2_f32 v[2:17], v29, v121, v[2:17]
	v_sub_f32_e32 v186, v186, v224
	v_min_f32_e32 v186, 0, v186
	v_mul_f32_e32 v186, 0x3fb8aa3b, v186
	v_exp_f32_e32 v186, v186
	v_mfma_f32_32x32x2_f32 v[2:17], v30, v122, v[2:17]
	v_or_b32_e32 v226, 18, v19
	v_mul_f32_e32 v186, v202, v186
	v_cmp_le_u32_e32 vcc, v18, v226
	v_mul_f32_e32 v186, v225, v186
	v_mfma_f32_32x32x2_f32 v[2:17], v31, v123, v[2:17]
	s_nop 0
	v_cndmask_b32_e32 v186, 0, v186, vcc
	v_sub_f32_e32 v187, v187, v224
	v_min_f32_e32 v187, 0, v187
	ds_read_b128 v[28:31], v32 offset:288
	ds_read_b128 v[120:123], v33 offset:288
	s_waitcnt lgkmcnt(2)
	v_mfma_f32_32x32x2_f32 v[2:17], v20, v24, v[2:17]
	v_mul_f32_e32 v187, 0x3fb8aa3b, v187
	v_exp_f32_e32 v187, v187
	v_or_b32_e32 v226, 19, v19
	v_mul_f32_e32 v187, v203, v187
	v_mfma_f32_32x32x2_f32 v[2:17], v21, v25, v[2:17]
	v_cmp_le_u32_e32 vcc, v18, v226
	v_mul_f32_e32 v187, v225, v187
	s_nop 0
	v_cndmask_b32_e32 v187, 0, v187, vcc
	v_mfma_f32_32x32x2_f32 v[2:17], v22, v26, v[2:17]
	v_sub_f32_e32 v188, v188, v224
	v_min_f32_e32 v188, 0, v188
	v_mul_f32_e32 v188, 0x3fb8aa3b, v188
	v_exp_f32_e32 v188, v188
	v_mfma_f32_32x32x2_f32 v[2:17], v23, v27, v[2:17]
	v_or_b32_e32 v226, 24, v19
	v_mul_f32_e32 v188, v204, v188
	v_cmp_le_u32_e32 vcc, v18, v226
	v_mul_f32_e32 v188, v225, v188
	ds_read_b128 v[20:23], v32 offset:320
	ds_read_b128 v[24:27], v33 offset:320
	s_waitcnt lgkmcnt(2)
	v_mfma_f32_32x32x2_f32 v[2:17], v28, v120, v[2:17]
	s_nop 0
	v_cndmask_b32_e32 v188, 0, v188, vcc
	v_sub_f32_e32 v189, v189, v224
	v_min_f32_e32 v189, 0, v189
	v_mfma_f32_32x32x2_f32 v[2:17], v29, v121, v[2:17]
	v_mul_f32_e32 v189, 0x3fb8aa3b, v189
	v_exp_f32_e32 v189, v189
	v_or_b32_e32 v226, 25, v19
	v_mul_f32_e32 v189, v205, v189
	v_mfma_f32_32x32x2_f32 v[2:17], v30, v122, v[2:17]
	v_cmp_le_u32_e32 vcc, v18, v226
	v_mul_f32_e32 v189, v225, v189
	s_nop 0
	v_cndmask_b32_e32 v189, 0, v189, vcc
	v_mfma_f32_32x32x2_f32 v[2:17], v31, v123, v[2:17]
	v_sub_f32_e32 v190, v190, v224
	v_min_f32_e32 v190, 0, v190
	v_mul_f32_e32 v190, 0x3fb8aa3b, v190
	v_exp_f32_e32 v190, v190
	ds_read_b128 v[28:31], v32 offset:352
	ds_read_b128 v[120:123], v33 offset:352
	s_waitcnt lgkmcnt(2)
	v_mfma_f32_32x32x2_f32 v[2:17], v20, v24, v[2:17]
	v_or_b32_e32 v226, 26, v19
	v_mul_f32_e32 v190, v206, v190
	v_cmp_le_u32_e32 vcc, v18, v226
	v_mul_f32_e32 v190, v225, v190
	v_mfma_f32_32x32x2_f32 v[2:17], v21, v25, v[2:17]
	s_nop 0
	v_cndmask_b32_e32 v190, 0, v190, vcc
	v_sub_f32_e32 v191, v191, v224
	v_min_f32_e32 v191, 0, v191
	v_mfma_f32_32x32x2_f32 v[2:17], v22, v26, v[2:17]
	v_mul_f32_e32 v191, 0x3fb8aa3b, v191
	v_exp_f32_e32 v191, v191
	v_or_b32_e32 v226, 27, v19
	v_mul_f32_e32 v191, v207, v191
	v_mfma_f32_32x32x2_f32 v[2:17], v23, v27, v[2:17]
	v_cmp_le_u32_e32 vcc, v18, v226
	v_mul_f32_e32 v191, v225, v191
	s_nop 0
	v_cndmask_b32_e32 v191, 0, v191, vcc
	s_waitcnt lgkmcnt(0)
	v_mfma_f32_32x32x2_f32 v[2:17], v28, v120, v[2:17]
	v_mfma_f32_32x32x2_f32 v[2:17], v29, v121, v[2:17]
	v_mfma_f32_32x32x2_f32 v[2:17], v30, v122, v[2:17]
	v_mfma_f32_32x32x2_f32 v[2:17], v31, v123, v[2:17]
	s_and_b64 vcc, exec, s[6:7]
	s_cbranch_vccz .Lp2_amt
	v_mad_u32_u24 v227, v19, s3, v227
	v_add_u32_e32 v227, v170, v227
	v_mul_f32_e32 v176, 0x3dd105ec, v176
	v_mul_f32_e32 v177, 0x3dd105ec, v177
	v_mul_f32_e32 v178, 0x3dd105ec, v178
	v_mul_f32_e32 v179, 0x3dd105ec, v179
	v_mul_f32_e32 v180, 0x3dd105ec, v180
	v_mul_f32_e32 v181, 0x3dd105ec, v181
	v_mul_f32_e32 v182, 0x3dd105ec, v182
	v_mul_f32_e32 v183, 0x3dd105ec, v183
	v_mul_f32_e32 v184, 0x3dd105ec, v184
	v_mul_f32_e32 v185, 0x3dd105ec, v185
	v_mul_f32_e32 v186, 0x3dd105ec, v186
	v_mul_f32_e32 v187, 0x3dd105ec, v187
	v_mul_f32_e32 v188, 0x3dd105ec, v188
	v_mul_f32_e32 v189, 0x3dd105ec, v189
	v_mul_f32_e32 v190, 0x3dd105ec, v190
	v_mul_f32_e32 v191, 0x3dd105ec, v191
	s_nop 7
	v_mul_f32_e32 v176, v2, v176
	v_mul_f32_e32 v177, v3, v177
	v_mul_f32_e32 v178, v4, v178
	v_mul_f32_e32 v179, v5, v179
	v_mul_f32_e32 v180, v6, v180
	v_mul_f32_e32 v181, v7, v181
	v_mul_f32_e32 v182, v8, v182
	v_mul_f32_e32 v183, v9, v183
	v_mul_f32_e32 v184, v10, v184
	v_mul_f32_e32 v185, v11, v185
	v_mul_f32_e32 v186, v12, v186
	v_mul_f32_e32 v187, v13, v187
	v_mul_f32_e32 v188, v14, v188
	v_mul_f32_e32 v189, v15, v189
	v_mul_f32_e32 v190, v16, v190
	v_mul_f32_e32 v191, v17, v191
	ds_write_b32 v227, v176
	ds_write_b32 v227, v177 offset:272
	ds_write_b32 v227, v178 offset:544
	ds_write_b32 v227, v179 offset:816
	ds_write_b32 v227, v180 offset:2176
	ds_write_b32 v227, v181 offset:2448
	ds_write_b32 v227, v182 offset:2720
	ds_write_b32 v227, v183 offset:2992
	ds_write_b32 v227, v184 offset:4352
	ds_write_b32 v227, v185 offset:4624
	ds_write_b32 v227, v186 offset:4896
	ds_write_b32 v227, v187 offset:5168
	ds_write_b32 v227, v188 offset:6528
	ds_write_b32 v227, v189 offset:6800
	ds_write_b32 v227, v190 offset:7072
	ds_write_b32 v227, v191 offset:7344
	s_branch .Lp2_done
.Lp2_amt:
	v_lshlrev_b32_e32 v226, 2, v19
	v_add_u32_e32 v228, v119, v226
	ds_read_b128 v[208:211], v228 offset:0
	ds_read_b128 v[212:215], v228 offset:32
	ds_read_b128 v[216:219], v228 offset:64
	ds_read_b128 v[220:223], v228 offset:96
	v_mad_u32_u24 v227, v18, s3, v226
	v_add_u32_e32 v227, v175, v227
	s_waitcnt lgkmcnt(0)
	v_mul_f32_e32 v176, v176, v208
	v_mul_f32_e32 v177, v177, v209
	v_mul_f32_e32 v178, v178, v210
	v_mul_f32_e32 v179, v179, v211
	v_mul_f32_e32 v180, v180, v212
	v_mul_f32_e32 v181, v181, v213
	v_mul_f32_e32 v182, v182, v214
	v_mul_f32_e32 v183, v183, v215
	v_mul_f32_e32 v184, v184, v216
	v_mul_f32_e32 v185, v185, v217
	v_mul_f32_e32 v186, v186, v218
	v_mul_f32_e32 v187, v187, v219
	v_mul_f32_e32 v188, v188, v220
	v_mul_f32_e32 v189, v189, v221
	v_mul_f32_e32 v190, v190, v222
	v_mul_f32_e32 v191, v191, v223
	v_mul_f32_e64 v176, v176, -v2
	v_mul_f32_e64 v177, v177, -v3
	v_mul_f32_e64 v178, v178, -v4
	v_mul_f32_e64 v179, v179, -v5
	v_mul_f32_e64 v180, v180, -v6
	v_mul_f32_e64 v181, v181, -v7
	v_mul_f32_e64 v182, v182, -v8
	v_mul_f32_e64 v183, v183, -v9
	v_mul_f32_e64 v184, v184, -v10
	v_mul_f32_e64 v185, v185, -v11
	v_mul_f32_e64 v186, v186, -v12
	v_mul_f32_e64 v187, v187, -v13
	v_mul_f32_e64 v188, v188, -v14
	v_mul_f32_e64 v189, v189, -v15
	v_mul_f32_e64 v190, v190, -v16
	v_mul_f32_e64 v191, v191, -v17
	v_mov_b32_e32 v232, v19
	v_or_b32_e32 v233, 1, v19
	v_or_b32_e32 v234, 2, v19
	v_or_b32_e32 v235, 3, v19
	v_cmp_lt_u32_e64 s[36:37], v18, v232
	v_cmp_lt_u32_e64 s[38:39], v18, v233
	v_cmp_lt_u32_e64 s[40:41], v18, v234
	v_cmp_lt_u32_e64 s[42:43], v18, v235
	s_nop 1
	v_cndmask_b32_e64 v176, 0, v176, s[36:37]
	v_cndmask_b32_e64 v177, 0, v177, s[38:39]
	v_cndmask_b32_e64 v178, 0, v178, s[40:41]
	v_cndmask_b32_e64 v179, 0, v179, s[42:43]
	ds_write_b128 v227, v[176:179]
	v_or_b32_e32 v232, 8, v19
	v_or_b32_e32 v233, 9, v19
	v_or_b32_e32 v234, 10, v19
	v_or_b32_e32 v235, 11, v19
	v_cmp_lt_u32_e64 s[36:37], v18, v232
	v_cmp_lt_u32_e64 s[38:39], v18, v233
	v_cmp_lt_u32_e64 s[40:41], v18, v234
	v_cmp_lt_u32_e64 s[42:43], v18, v235
	s_nop 1
	v_cndmask_b32_e64 v180, 0, v180, s[36:37]
	v_cndmask_b32_e64 v181, 0, v181, s[38:39]
	v_cndmask_b32_e64 v182, 0, v182, s[40:41]
	v_cndmask_b32_e64 v183, 0, v183, s[42:43]
	ds_write_b128 v227, v[180:183] offset:32
	v_or_b32_e32 v232, 16, v19
	v_or_b32_e32 v233, 17, v19
	v_or_b32_e32 v234, 18, v19
	v_or_b32_e32 v235, 19, v19
	v_cmp_lt_u32_e64 s[36:37], v18, v232
	v_cmp_lt_u32_e64 s[38:39], v18, v233
	v_cmp_lt_u32_e64 s[40:41], v18, v234
	v_cmp_lt_u32_e64 s[42:43], v18, v235
	s_nop 1
	v_cndmask_b32_e64 v184, 0, v184, s[36:37]
	v_cndmask_b32_e64 v185, 0, v185, s[38:39]
	v_cndmask_b32_e64 v186, 0, v186, s[40:41]
	v_cndmask_b32_e64 v187, 0, v187, s[42:43]
	ds_write_b128 v227, v[184:187] offset:64
	v_or_b32_e32 v232, 24, v19
	v_or_b32_e32 v233, 25, v19
	v_or_b32_e32 v234, 26, v19
	v_or_b32_e32 v235, 27, v19
	v_cmp_lt_u32_e64 s[36:37], v18, v232
	v_cmp_lt_u32_e64 s[38:39], v18, v233
	v_cmp_lt_u32_e64 s[40:41], v18, v234
	v_cmp_lt_u32_e64 s[42:43], v18, v235
	s_nop 1
	v_cndmask_b32_e64 v188, 0, v188, s[36:37]
	v_cndmask_b32_e64 v189, 0, v189, s[38:39]
	v_cndmask_b32_e64 v190, 0, v190, s[40:41]
	v_cndmask_b32_e64 v191, 0, v191, s[42:43]
	ds_write_b128 v227, v[188:191] offset:96
.Lp2_done:
.LBB1_123:
	s_or_b64 exec, exec, s[0:1]
	s_movk_i32 s0, 0x120
	v_cmp_gt_u32_e32 vcc, s0, v0
	s_movk_i32 s0, 0x11f
	v_cmp_lt_u32_e64 s[0:1], s0, v0
	s_waitcnt lgkmcnt(0)
	s_barrier
	s_and_saveexec_b64 s[10:11], s[0:1]
	s_xor_b64 s[0:1], exec, s[10:11]
	s_cbranch_execz .LBB1_125
	v_mov_b32_e32 v130, v82
	v_mov_b32_e32 v128, v80
	v_mov_b32_e32 v126, v78
	v_mov_b32_e32 v124, v76
	v_mov_b32_e32 v122, v74
	v_mov_b32_e32 v120, v72
	v_mov_b32_e32 v118, v70
	v_mov_b32_e32 v116, v68
	v_mov_b64_e32 v[64:65], v[82:83]
	v_mov_b64_e32 v[60:61], v[80:81]
	v_mov_b64_e32 v[56:57], v[78:79]
	v_mov_b64_e32 v[52:53], v[76:77]
	v_mov_b64_e32 v[48:49], v[74:75]
	v_mov_b64_e32 v[44:45], v[72:73]
	v_mov_b64_e32 v[40:41], v[70:71]
	v_mov_b64_e32 v[36:37], v[68:69]

	.amdhsa_kernel _Z11prep_kernel8PrepArgs
		.amdhsa_group_segment_fixed_size 149760
		.amdhsa_private_segment_fixed_size 0
		.amdhsa_kernarg_size 96
		.amdhsa_user_sgpr_count 2
		.amdhsa_user_sgpr_dispatch_ptr 0
		.amdhsa_user_sgpr_queue_ptr 0
		.amdhsa_user_sgpr_kernarg_segment_ptr 1
		.amdhsa_user_sgpr_dispatch_id 0
		.amdhsa_user_sgpr_kernarg_preload_length 0
		.amdhsa_user_sgpr_kernarg_preload_offset 0
		.amdhsa_user_sgpr_private_segment_size 0
		.amdhsa_uses_dynamic_stack 0
		.amdhsa_enable_private_segment 0
		.amdhsa_system_sgpr_workgroup_id_x 1
		.amdhsa_system_sgpr_workgroup_id_y 0
		.amdhsa_system_sgpr_workgroup_id_z 0
		.amdhsa_system_sgpr_workgroup_info 0
		.amdhsa_system_vgpr_workitem_id 0
		.amdhsa_next_free_vgpr 256
		.amdhsa_next_free_sgpr 96
		.amdhsa_accum_offset 256
		.amdhsa_reserve_vcc 1
		.amdhsa_float_round_mode_32 0
		.amdhsa_float_round_mode_16_64 0
		.amdhsa_float_denorm_mode_32 3
		.amdhsa_float_denorm_mode_16_64 3
		.amdhsa_dx10_clamp 1
		.amdhsa_ieee_mode 1
		.amdhsa_fp16_overflow 0
		.amdhsa_tg_split 0
		.amdhsa_exception_fp_ieee_invalid_op 0
		.amdhsa_exception_fp_denorm_src 0
		.amdhsa_exception_fp_ieee_div_zero 0
		.amdhsa_exception_fp_ieee_overflow 0
		.amdhsa_exception_fp_ieee_underflow 0
		.amdhsa_exception_fp_ieee_inexact 0
		.amdhsa_exception_int_div_zero 0
	.end_amdhsa_kernel

	.amdhsa_kernel _Z8gemm_f16ILi128ELi64ELi2ELi2ELi4ELi2ELi0EEvPKDF16_S1_Pviiii
		.amdhsa_group_segment_fixed_size 98304
		.amdhsa_private_segment_fixed_size 0
		.amdhsa_kernarg_size 40
		.amdhsa_user_sgpr_count 2
		.amdhsa_user_sgpr_dispatch_ptr 0
		.amdhsa_user_sgpr_queue_ptr 0
		.amdhsa_user_sgpr_kernarg_segment_ptr 1
		.amdhsa_user_sgpr_dispatch_id 0
		.amdhsa_user_sgpr_kernarg_preload_length 0
		.amdhsa_user_sgpr_kernarg_preload_offset 0
		.amdhsa_user_sgpr_private_segment_size 0
		.amdhsa_uses_dynamic_stack 0
		.amdhsa_enable_private_segment 0
		.amdhsa_system_sgpr_workgroup_id_x 1
		.amdhsa_system_sgpr_workgroup_id_y 0
		.amdhsa_system_sgpr_workgroup_id_z 0
		.amdhsa_system_sgpr_workgroup_info 0
		.amdhsa_system_vgpr_workitem_id 0
		.amdhsa_next_free_vgpr 96
		.amdhsa_next_free_sgpr 96
		.amdhsa_accum_offset 64
		.amdhsa_reserve_vcc 0
		.amdhsa_float_round_mode_32 0
		.amdhsa_float_round_mode_16_64 0
		.amdhsa_float_denorm_mode_32 3
		.amdhsa_float_denorm_mode_16_64 3
		.amdhsa_dx10_clamp 1
		.amdhsa_ieee_mode 1
		.amdhsa_fp16_overflow 0
		.amdhsa_tg_split 0
		.amdhsa_exception_fp_ieee_invalid_op 0
		.amdhsa_exception_fp_denorm_src 0
		.amdhsa_exception_fp_ieee_div_zero 0
		.amdhsa_exception_fp_ieee_overflow 0
		.amdhsa_exception_fp_ieee_underflow 0
		.amdhsa_exception_fp_ieee_inexact 0
		.amdhsa_exception_int_div_zero 0
	.end_amdhsa_kernel

amdhsa.kernels:
  - .agpr_count:     0
    .args:
      - .offset:         0
        .size:           88
        .value_kind:     by_value
    .group_segment_fixed_size: 16640
    .kernarg_segment_align: 8
    .kernarg_segment_size: 88
    .language:       OpenCL C
    .language_version:
      - 2
      - 0
    .max_flat_workgroup_size: 256
    .name:           _Z15prologue_kernel7ProArgs
    .private_segment_fixed_size: 0
    .sgpr_count:     28
    .sgpr_spill_count: 0
    .symbol:         _Z15prologue_kernel7ProArgs.kd
    .uniform_work_group_size: 1
    .uses_dynamic_stack: false
    .vgpr_count:     54
    .vgpr_spill_count: 0
    .wavefront_size: 64
  - .agpr_count:     0
    .args:
      - .offset:         0
        .size:           96
        .value_kind:     by_value
    .group_segment_fixed_size: 149760
    .kernarg_segment_align: 8
    .kernarg_segment_size: 96
    .language:       OpenCL C
    .language_version:
      - 2
      - 0
    .max_flat_workgroup_size: 384
    .name:           _Z11prep_kernel8PrepArgs
    .private_segment_fixed_size: 0
    .sgpr_count:     41
    .sgpr_spill_count: 0
    .symbol:         _Z11prep_kernel8PrepArgs.kd
    .uniform_work_group_size: 1
    .uses_dynamic_stack: false
    .vgpr_count:     256
    .vgpr_spill_count: 0
    .wavefront_size: 64
  - .agpr_count:     0
    .args:
      - .actual_access:  read_only
        .address_space:  global
        .offset:         0
        .size:           8
        .value_kind:     global_buffer
      - .actual_access:  read_only
        .address_space:  global
        .offset:         8
        .size:           8
        .value_kind:     global_buffer
      - .actual_access:  read_only
        .address_space:  global
        .offset:         16
        .size:           8
        .value_kind:     global_buffer
      - .actual_access:  read_only
        .address_space:  global
        .offset:         24
        .size:           8
        .value_kind:     global_buffer
      - .actual_access:  write_only
        .address_space:  global
        .offset:         32
        .size:           8
        .value_kind:     global_buffer
      - .actual_access:  write_only
        .address_space:  global
        .offset:         40
        .size:           8
        .value_kind:     global_buffer
    .group_segment_fixed_size: 0
    .kernarg_segment_align: 8
    .kernarg_segment_size: 48
    .language:       OpenCL C
    .language_version:
      - 2
      - 0
    .max_flat_workgroup_size: 64
    .name:           _Z16rec_chunk_kernelPKDF16_PKfS2_S2_PfS3_
    .private_segment_fixed_size: 0
    .sgpr_count:     42
    .sgpr_spill_count: 0
    .symbol:         _Z16rec_chunk_kernelPKDF16_PKfS2_S2_PfS3_.kd
    .uniform_work_group_size: 1
    .uses_dynamic_stack: false
    .vgpr_count:     256
    .vgpr_spill_count: 0
    .wavefront_size: 64
  - .agpr_count:     0
    .args:
      - .actual_access:  read_only
        .address_space:  global
        .offset:         0
        .size:           8
        .value_kind:     global_buffer
      - .actual_access:  read_only
        .address_space:  global
        .offset:         8
        .size:           8
        .value_kind:     global_buffer
      - .actual_access:  read_only
        .address_space:  global
        .offset:         16
        .size:           8
        .value_kind:     global_buffer
      - .actual_access:  write_only
        .address_space:  global
        .offset:         24
        .size:           8
        .value_kind:     global_buffer
      - .actual_access:  read_only
        .address_space:  global
        .offset:         32
        .size:           8
        .value_kind:     global_buffer
      - .actual_access:  write_only
        .address_space:  global
        .offset:         40
        .size:           8
        .value_kind:     global_buffer
    .group_segment_fixed_size: 16640
    .kernarg_segment_align: 8
    .kernarg_segment_size: 48
    .language:       OpenCL C
    .language_version:
      - 2
      - 0
    .max_flat_workgroup_size: 256
    .name:           _Z16norm_gate_kernelPKfPKDF16_S0_PDF16_S0_S3_
    .private_segment_fixed_size: 0
    .sgpr_count:     20
    .sgpr_spill_count: 0
    .symbol:         _Z16norm_gate_kernelPKfPKDF16_S0_PDF16_S0_S3_.kd
    .uniform_work_group_size: 1
    .uses_dynamic_stack: false
    .vgpr_count:     63
    .vgpr_spill_count: 0
    .wavefront_size: 64
  - .agpr_count:     0
    .args:
      - .address_space:  global
        .offset:         0
        .size:           8
        .value_kind:     global_buffer
      - .address_space:  global
        .offset:         8
        .size:           8
        .value_kind:     global_buffer
      - .actual_access:  write_only
        .address_space:  global
        .offset:         16
        .size:           8
        .value_kind:     global_buffer
      - .offset:         24
        .size:           4
        .value_kind:     by_value
      - .offset:         28
        .size:           4
        .value_kind:     by_value
      - .offset:         32
        .size:           4
        .value_kind:     by_value
      - .offset:         36
        .size:           4
        .value_kind:     by_value
    .group_segment_fixed_size: 106496
    .kernarg_segment_align: 8
    .kernarg_segment_size: 40
    .language:       OpenCL C
    .language_version:
      - 2
      - 0
    .max_flat_workgroup_size: 512
    .name:           _Z8gemm_f16ILi256ELi160ELi4ELi2ELi2ELi1ELi1EEvPKDF16_S1_Pviiii
    .private_segment_fixed_size: 0
    .sgpr_count:     22
    .sgpr_spill_count: 0
    .symbol:         _Z8gemm_f16ILi256ELi160ELi4ELi2ELi2ELi1ELi1EEvPKDF16_S1_Pviiii.kd
    .uniform_work_group_size: 1
    .uses_dynamic_stack: false
    .vgpr_count:     140
    .vgpr_spill_count: 0
    .wavefront_size: 64
  - .agpr_count:     32
    .args:
      - .address_space:  global
        .offset:         0
        .size:           8
        .value_kind:     global_buffer
      - .address_space:  global
        .offset:         8
        .size:           8
        .value_kind:     global_buffer
      - .actual_access:  write_only
        .address_space:  global
        .offset:         16
        .size:           8
        .value_kind:     global_buffer
      - .offset:         24
        .size:           4
        .value_kind:     by_value
      - .offset:         28
        .size:           4
        .value_kind:     by_value
      - .offset:         32
        .size:           4
        .value_kind:     by_value
      - .offset:         36
        .size:           4
        .value_kind:     by_value
    .group_segment_fixed_size: 98304
    .kernarg_segment_align: 8
    .kernarg_segment_size: 40
    .language:       OpenCL C
    .language_version:
      - 2
      - 0
    .max_flat_workgroup_size: 256
    .name:           _Z8gemm_f16ILi128ELi64ELi2ELi2ELi4ELi2ELi0EEvPKDF16_S1_Pviiii
    .private_segment_fixed_size: 0
    .sgpr_count:     25
    .sgpr_spill_count: 0
    .symbol:         _Z8gemm_f16ILi128ELi64ELi2ELi2ELi4ELi2ELi0EEvPKDF16_S1_Pviiii.kd
    .uniform_work_group_size: 1
    .uses_dynamic_stack: false
    .vgpr_count:     96
    .vgpr_spill_count: 0
    .wavefront_size: 64
